# baseline (speedup 1.0000x reference)
_Z8gemm16_kILi128ELi128ELi1ELi3EEvPKDF16_S1_PvPKfi:
	s_load_dwordx8 s[4:11], s[0:1], 0x0
	v_readfirstlane_b32 s3, v0
	s_cmpk_lt_i32 s3, 0x100
	s_cbranch_scc1 .LBB3_2
	s_nop 0
